# baseline (speedup 1.0000x reference)
.LBB2_1:
	s_mov_b32 s17, s31
	s_mov_b32 s18, s15
	v_add_u32_e32 v185, s18, v181
	ds_read_b64_tr_b16 v[176:177], v185 offset:24576
	ds_read_b64_tr_b16 v[178:179], v185 offset:25088
	v_mfma_f32_32x32x16_f16 v[96:111], v[172:175], v[136:139], v[0:15]
	v_add_f32_e32 v80, v64, v65
	v_add_f32_e32 v80, v66, v80
	v_add_f32_e32 v80, v67, v80
	v_add_f32_e32 v80, v68, v80
	v_add_f32_e32 v80, v69, v80
	v_cvt_pk_f16_f32 v140, v64, v65
	v_cvt_pk_f16_f32 v141, v66, v67
	ds_read_b64_tr_b16 v[172:173], v185 offset:28672
	ds_read_b64_tr_b16 v[174:175], v185 offset:29184
	v_add_f32_e32 v64, v70, v80
	v_mfma_f32_32x32x16_f16 v[80:95], v[168:171], v[136:139], v[0:15]
	v_add_f32_e32 v64, v71, v64
	v_add_f32_e32 v64, v72, v64
	v_add_f32_e32 v64, v73, v64
	v_cvt_pk_f16_f32 v142, v68, v69
	v_cvt_pk_f16_f32 v143, v70, v71
	ds_read_b64_tr_b16 v[68:69], v185 offset:25600
	ds_read_b64_tr_b16 v[70:71], v185 offset:26112
	v_mfma_f32_32x32x16_f16 v[96:111], v[164:167], v[128:131], v[96:111]
	v_add_f32_e32 v64, v74, v64
	v_add_f32_e32 v64, v75, v64
	v_add_f32_e32 v64, v76, v64
	v_add_f32_e32 v116, v77, v64
	v_cvt_pk_f16_f32 v132, v72, v73
	v_cvt_pk_f16_f32 v133, v74, v75
	ds_read_b64_tr_b16 v[64:65], v185 offset:29696
	ds_read_b64_tr_b16 v[66:67], v185 offset:30208
	v_mfma_f32_32x32x16_f16 v[80:95], v[160:163], v[128:131], v[80:95]
	v_add_f32_e32 v72, v78, v116
	v_add_f32_e32 v72, v79, v72
	v_add_f32_e32 v72, v48, v72
	v_add_f32_e32 v116, v49, v72
	v_cvt_pk_f16_f32 v134, v76, v77
	v_cvt_pk_f16_f32 v135, v78, v79
	ds_read_b64_tr_b16 v[72:73], v185 offset:26624
	ds_read_b64_tr_b16 v[74:75], v185 offset:27136
	v_mfma_f32_32x32x16_f16 v[96:111], v[156:159], v[120:123], v[96:111]
	v_add_f32_e32 v76, v50, v116
	v_add_f32_e32 v76, v51, v76
	v_add_f32_e32 v76, v52, v76
	v_add_f32_e32 v76, v53, v76
	v_cvt_pk_f16_f32 v124, v48, v49
	v_cvt_pk_f16_f32 v125, v50, v51
	ds_read_b64_tr_b16 v[48:49], v185 offset:30720
	ds_read_b64_tr_b16 v[50:51], v185 offset:31232
	v_mfma_f32_32x32x16_f16 v[80:95], v[152:155], v[120:123], v[80:95]
	v_add_f32_e32 v76, v54, v76
	v_add_f32_e32 v76, v55, v76
	v_add_f32_e32 v76, v56, v76
	v_add_f32_e32 v76, v57, v76
	v_cvt_pk_f16_f32 v126, v52, v53
	v_cvt_pk_f16_f32 v127, v54, v55
	ds_read_b64_tr_b16 v[52:53], v185 offset:27648
	ds_read_b64_tr_b16 v[54:55], v185 offset:28160
	v_mfma_f32_32x32x16_f16 v[96:111], v[148:151], v[112:115], v[96:111]
	v_add_f32_e32 v76, v58, v76
	v_add_f32_e32 v76, v59, v76
	v_add_f32_e32 v76, v60, v76
	v_add_f32_e32 v76, v61, v76
	v_cvt_pk_f16_f32 v116, v56, v57
	v_cvt_pk_f16_f32 v117, v58, v59
	ds_read_b64_tr_b16 v[56:57], v185 offset:31744
	ds_read_b64_tr_b16 v[58:59], v185 offset:32256
	v_mfma_f32_32x32x16_f16 v[80:95], v[144:147], v[112:115], v[80:95]
	v_add_f32_e32 v76, v62, v76
	v_add_f32_e32 v76, v63, v76
	v_cvt_pk_f16_f32 v118, v60, v61
	v_cvt_pk_f16_f32 v119, v62, v63
	s_add_i32 m0, s14, s25
	v_cmp_lt_f32_e32 vcc, s36, v76
	global_load_lds_dwordx4 v180, s[44:45]
	s_add_i32 m0, s28, s26
	s_add_u32 s44, s44, 0x2000
	global_load_lds_dwordx4 v180, s[46:47]
	s_addc_u32 s45, s45, 0
	s_add_u32 s46, s46, 0x2000
	s_addc_u32 s47, s47, 0
	s_cbranch_vccnz .Lmy_rare_1

.LBB2_2:
	s_waitcnt lgkmcnt(8)
	v_mfma_f32_32x32x16_f16 v[16:31], v[140:143], v[176:179], v[16:31]
	v_exp_f32_e32 v96, v96
	v_exp_f32_e32 v97, v97
	v_exp_f32_e32 v98, v98
	v_exp_f32_e32 v99, v99
	v_mfma_f32_32x32x16_f16 v[32:47], v[140:143], v[172:175], v[32:47]
	v_exp_f32_e32 v100, v100
	v_exp_f32_e32 v101, v101
	v_exp_f32_e32 v102, v102
	v_exp_f32_e32 v103, v103
	v_add_u32_e32 v76, s19, v184
	ds_read_b128 v[60:63], v76
	ds_read_b128 v[148:151], v76 offset:512
	v_mfma_f32_32x32x16_f16 v[16:31], v[132:135], v[68:71], v[16:31]
	v_exp_f32_e32 v104, v104
	v_exp_f32_e32 v105, v105
	v_exp_f32_e32 v106, v106
	v_exp_f32_e32 v107, v107
	ds_read_b128 v[176:179], v76 offset:2048
	ds_read_b128 v[172:175], v76 offset:2560
	v_mfma_f32_32x32x16_f16 v[32:47], v[132:135], v[64:67], v[32:47]
	v_exp_f32_e32 v108, v108
	v_exp_f32_e32 v109, v109
	v_exp_f32_e32 v110, v110
	v_exp_f32_e32 v111, v111
	ds_read_b128 v[168:171], v76 offset:4096
	ds_read_b128 v[164:167], v76 offset:4608
	s_waitcnt lgkmcnt(6)
	v_mfma_f32_32x32x16_f16 v[16:31], v[124:127], v[72:75], v[16:31]
	v_exp_f32_e32 v80, v80
	v_exp_f32_e32 v81, v81
	v_exp_f32_e32 v82, v82
	v_exp_f32_e32 v83, v83
	ds_read_b128 v[160:163], v76 offset:6144
	ds_read_b128 v[156:159], v76 offset:6656
	v_mfma_f32_32x32x16_f16 v[32:47], v[124:127], v[48:51], v[32:47]
	v_exp_f32_e32 v84, v84
	v_exp_f32_e32 v85, v85
	v_exp_f32_e32 v86, v86
	v_exp_f32_e32 v87, v87
	v_mfma_f32_32x32x16_f16 v[16:31], v[116:119], v[52:55], v[16:31]
	v_exp_f32_e32 v88, v88
	v_exp_f32_e32 v89, v89
	v_exp_f32_e32 v90, v90
	v_exp_f32_e32 v91, v91
	v_mfma_f32_32x32x16_f16 v[32:47], v[116:119], v[56:59], v[32:47]
	v_exp_f32_e32 v92, v92
	v_exp_f32_e32 v93, v93
	v_exp_f32_e32 v94, v94
	v_exp_f32_e32 v95, v95
	s_waitcnt vmcnt(3) lgkmcnt(0)
	s_barrier
.LBB2_4:
	v_add_u32_e32 v185, s17, v181
	ds_read_b64_tr_b16 v[144:145], v185 offset:24576
	ds_read_b64_tr_b16 v[146:147], v185 offset:25088
	v_mfma_f32_32x32x16_f16 v[64:79], v[60:63], v[136:139], v[0:15]
	v_add_f32_e32 v48, v96, v97
	v_add_f32_e32 v48, v98, v48
	v_add_f32_e32 v48, v99, v48
	v_add_f32_e32 v48, v100, v48
	v_add_f32_e32 v48, v101, v48
	v_cvt_pk_f16_f32 v140, v96, v97
	v_cvt_pk_f16_f32 v141, v98, v99
	ds_read_b64_tr_b16 v[152:153], v185 offset:28672
	ds_read_b64_tr_b16 v[154:155], v185 offset:29184
	v_add_f32_e32 v48, v102, v48
	v_add_f32_e32 v48, v103, v48
	v_add_f32_e32 v48, v104, v48
	v_add_f32_e32 v96, v105, v48
	v_mfma_f32_32x32x16_f16 v[48:63], v[148:151], v[136:139], v[0:15]
	v_cvt_pk_f16_f32 v142, v100, v101
	v_cvt_pk_f16_f32 v143, v102, v103
	ds_read_b64_tr_b16 v[148:149], v185 offset:25600
	ds_read_b64_tr_b16 v[150:151], v185 offset:26112
	v_mfma_f32_32x32x16_f16 v[64:79], v[176:179], v[128:131], v[64:79]
	v_add_f32_e32 v96, v106, v96
	v_add_f32_e32 v96, v107, v96
	v_add_f32_e32 v96, v108, v96
	v_add_f32_e32 v96, v109, v96
	v_cvt_pk_f16_f32 v132, v104, v105
	v_cvt_pk_f16_f32 v133, v106, v107
	ds_read_b64_tr_b16 v[100:101], v185 offset:29696
	ds_read_b64_tr_b16 v[102:103], v185 offset:30208
	v_mfma_f32_32x32x16_f16 v[48:63], v[172:175], v[128:131], v[48:63]
	v_add_f32_e32 v96, v110, v96
	v_add_f32_e32 v96, v111, v96
	v_add_f32_e32 v96, v80, v96
	v_add_f32_e32 v104, v81, v96
	v_cvt_pk_f16_f32 v134, v108, v109
	v_cvt_pk_f16_f32 v135, v110, v111
	ds_read_b64_tr_b16 v[96:97], v185 offset:26624
	ds_read_b64_tr_b16 v[98:99], v185 offset:27136
	v_mfma_f32_32x32x16_f16 v[64:79], v[168:171], v[120:123], v[64:79]
	v_add_f32_e32 v104, v82, v104
	v_add_f32_e32 v104, v83, v104
	v_add_f32_e32 v104, v84, v104
	v_add_f32_e32 v104, v85, v104
	v_cvt_pk_f16_f32 v124, v80, v81
	v_cvt_pk_f16_f32 v125, v82, v83
	ds_read_b64_tr_b16 v[80:81], v185 offset:30720
	ds_read_b64_tr_b16 v[82:83], v185 offset:31232
	v_mfma_f32_32x32x16_f16 v[48:63], v[164:167], v[120:123], v[48:63]
	v_add_f32_e32 v104, v86, v104
	v_add_f32_e32 v104, v87, v104
	v_add_f32_e32 v104, v88, v104
	v_add_f32_e32 v104, v89, v104
	v_cvt_pk_f16_f32 v126, v84, v85
	v_cvt_pk_f16_f32 v127, v86, v87
	ds_read_b64_tr_b16 v[84:85], v185 offset:27648
	ds_read_b64_tr_b16 v[86:87], v185 offset:28160
	v_mfma_f32_32x32x16_f16 v[64:79], v[160:163], v[112:115], v[64:79]
	v_add_f32_e32 v104, v90, v104
	v_add_f32_e32 v104, v91, v104
	v_add_f32_e32 v104, v92, v104
	v_add_f32_e32 v104, v93, v104
	v_cvt_pk_f16_f32 v116, v88, v89
	v_cvt_pk_f16_f32 v117, v90, v91
	ds_read_b64_tr_b16 v[88:89], v185 offset:31744
	ds_read_b64_tr_b16 v[90:91], v185 offset:32256
	v_mfma_f32_32x32x16_f16 v[48:63], v[156:159], v[112:115], v[48:63]
	v_add_f32_e32 v104, v94, v104
	v_add_f32_e32 v104, v95, v104
	v_cvt_pk_f16_f32 v118, v92, v93
	v_cvt_pk_f16_f32 v119, v94, v95
	s_add_i32 m0, s19, s25
	v_cmp_lt_f32_e32 vcc, s36, v104
	global_load_lds_dwordx4 v180, s[44:45]
	s_add_i32 m0, s18, s26
	s_add_u32 s44, s44, 0x2000
	global_load_lds_dwordx4 v180, s[46:47]
	s_addc_u32 s45, s45, 0
	s_add_u32 s46, s46, 0x2000
	s_addc_u32 s47, s47, 0
	s_cbranch_vccnz .Lmy_rare_2

.LBB2_5:
	s_add_i32 s14, s19, 0x2000
	s_cmpk_lg_i32 s19, 0x4000
	s_cselect_b32 s14, s14, 0
	s_waitcnt lgkmcnt(8)
	v_mfma_f32_32x32x16_f16 v[16:31], v[140:143], v[144:147], v[16:31]
	v_exp_f32_e32 v64, v64
	v_exp_f32_e32 v65, v65
	v_exp_f32_e32 v66, v66
	v_exp_f32_e32 v67, v67
	v_mfma_f32_32x32x16_f16 v[32:47], v[140:143], v[152:155], v[32:47]
	v_exp_f32_e32 v68, v68
	v_exp_f32_e32 v69, v69
	v_exp_f32_e32 v70, v70
	v_exp_f32_e32 v71, v71
	v_add_u32_e32 v92, s14, v184
	ds_read_b128 v[172:175], v92
	ds_read_b128 v[168:171], v92 offset:512
	v_mfma_f32_32x32x16_f16 v[16:31], v[132:135], v[148:151], v[16:31]
	v_exp_f32_e32 v72, v72
	v_exp_f32_e32 v73, v73
	v_exp_f32_e32 v74, v74
	v_exp_f32_e32 v75, v75
	ds_read_b128 v[164:167], v92 offset:2048
	ds_read_b128 v[160:163], v92 offset:2560
	v_mfma_f32_32x32x16_f16 v[32:47], v[132:135], v[100:103], v[32:47]
	v_exp_f32_e32 v76, v76
	v_exp_f32_e32 v77, v77
	v_exp_f32_e32 v78, v78
	v_exp_f32_e32 v79, v79
	ds_read_b128 v[156:159], v92 offset:4096
	ds_read_b128 v[152:155], v92 offset:4608
	s_waitcnt lgkmcnt(6)
	v_mfma_f32_32x32x16_f16 v[16:31], v[124:127], v[96:99], v[16:31]
	v_exp_f32_e32 v48, v48
	v_exp_f32_e32 v49, v49
	v_exp_f32_e32 v50, v50
	v_exp_f32_e32 v51, v51
	ds_read_b128 v[148:151], v92 offset:6144
	ds_read_b128 v[144:147], v92 offset:6656
	v_mfma_f32_32x32x16_f16 v[32:47], v[124:127], v[80:83], v[32:47]
	v_exp_f32_e32 v52, v52
	v_exp_f32_e32 v53, v53
	v_exp_f32_e32 v54, v54
	v_exp_f32_e32 v55, v55
	v_mfma_f32_32x32x16_f16 v[16:31], v[116:119], v[84:87], v[16:31]
	v_exp_f32_e32 v56, v56
	v_exp_f32_e32 v57, v57
	v_exp_f32_e32 v58, v58
	v_exp_f32_e32 v59, v59
	v_mfma_f32_32x32x16_f16 v[32:47], v[116:119], v[88:91], v[32:47]
	v_exp_f32_e32 v60, v60
	v_exp_f32_e32 v61, v61
	v_exp_f32_e32 v62, v62
	v_exp_f32_e32 v63, v63
	s_add_i32 s6, s14, 0x2000
	s_cmpk_lg_i32 s14, 0x4000
	s_cselect_b32 s19, s6, 0
	s_add_i32 s27, s27, 2
	s_mov_b32 s15, s29
	s_mov_b32 s31, s28
	s_mov_b32 s29, s18
	s_mov_b32 s28, s17
	s_cmp_gt_u32 s27, 28
	s_waitcnt vmcnt(3) lgkmcnt(0)
	s_barrier
	s_cbranch_scc0 .LBB2_1
.LBB2_15:
	ds_read_b64_tr_b16 v[96:97], v181 offset:40960
	ds_read_b64_tr_b16 v[98:99], v181 offset:41472
	v_add_f32_e32 v80, v64, v65
	v_add_f32_e32 v80, v66, v80
	v_add_f32_e32 v80, v67, v80
	v_add_f32_e32 v80, v68, v80
	v_add_f32_e32 v100, v69, v80
	v_mfma_f32_32x32x16_f16 v[80:95], v[172:175], v[136:139], v[0:15]
	v_cvt_pk_f16_f32 v140, v64, v65
	v_cvt_pk_f16_f32 v141, v66, v67
	ds_read_b64_tr_b16 v[64:65], v181 offset:45056
	ds_read_b64_tr_b16 v[66:67], v181 offset:45568
	v_mfma_f32_32x32x16_f16 v[0:15], v[168:171], v[136:139], v[0:15]
	v_add_f32_e32 v100, v70, v100
	v_add_f32_e32 v100, v71, v100
	v_add_f32_e32 v100, v72, v100
	v_add_f32_e32 v100, v73, v100
	v_cvt_pk_f16_f32 v142, v68, v69
	v_cvt_pk_f16_f32 v143, v70, v71
	ds_read_b64_tr_b16 v[68:69], v181 offset:41984
	ds_read_b64_tr_b16 v[70:71], v181 offset:42496
	v_mfma_f32_32x32x16_f16 v[80:95], v[164:167], v[128:131], v[80:95]
	v_add_f32_e32 v100, v74, v100
	v_add_f32_e32 v100, v75, v100
	v_add_f32_e32 v100, v76, v100
	v_add_f32_e32 v100, v77, v100
	v_cvt_pk_f16_f32 v132, v72, v73
	v_cvt_pk_f16_f32 v133, v74, v75
	ds_read_b64_tr_b16 v[72:73], v181 offset:46080
	ds_read_b64_tr_b16 v[74:75], v181 offset:46592
	v_mfma_f32_32x32x16_f16 v[0:15], v[160:163], v[128:131], v[0:15]
	v_add_f32_e32 v100, v78, v100
	v_add_f32_e32 v100, v79, v100
	v_add_f32_e32 v100, v48, v100
	v_add_f32_e32 v100, v49, v100
	v_cvt_pk_f16_f32 v134, v76, v77
	v_cvt_pk_f16_f32 v135, v78, v79
	ds_read_b64_tr_b16 v[76:77], v181 offset:43008
	ds_read_b64_tr_b16 v[78:79], v181 offset:43520
	v_mfma_f32_32x32x16_f16 v[80:95], v[156:159], v[120:123], v[80:95]
	v_add_f32_e32 v100, v50, v100
	v_add_f32_e32 v100, v51, v100
	v_add_f32_e32 v100, v52, v100
	v_add_f32_e32 v104, v53, v100
	v_cvt_pk_f16_f32 v124, v48, v49
	v_cvt_pk_f16_f32 v125, v50, v51
	ds_read_b64_tr_b16 v[100:101], v181 offset:47104
	ds_read_b64_tr_b16 v[102:103], v181 offset:47616
	v_mfma_f32_32x32x16_f16 v[0:15], v[152:155], v[120:123], v[0:15]
	v_add_f32_e32 v48, v54, v104
	v_add_f32_e32 v48, v55, v48
	v_add_f32_e32 v48, v56, v48
	v_add_f32_e32 v48, v57, v48
	v_cvt_pk_f16_f32 v126, v52, v53
	v_cvt_pk_f16_f32 v127, v54, v55
	ds_read_b64_tr_b16 v[104:105], v181 offset:44032
	ds_read_b64_tr_b16 v[106:107], v181 offset:44544
	v_mfma_f32_32x32x16_f16 v[80:95], v[148:151], v[112:115], v[80:95]
	v_add_f32_e32 v48, v58, v48
	v_add_f32_e32 v48, v59, v48
	v_add_f32_e32 v48, v60, v48
	v_add_f32_e32 v48, v61, v48
	v_cvt_pk_f16_f32 v116, v56, v57
	v_cvt_pk_f16_f32 v117, v58, v59
	ds_read_b64_tr_b16 v[108:109], v181 offset:48128
	ds_read_b64_tr_b16 v[110:111], v181 offset:48640
	v_mfma_f32_32x32x16_f16 v[0:15], v[144:147], v[112:115], v[0:15]
	v_add_f32_e32 v48, v62, v48
	v_add_f32_e32 v48, v63, v48
	v_cvt_pk_f16_f32 v118, v60, v61
	v_cvt_pk_f16_f32 v119, v62, v63
	s_nop 0
	v_cmp_lt_f32_e32 vcc, s36, v48
	s_nop 4
	s_cbranch_vccnz .Lmy_rare_3

.LBB2_16:
	s_waitcnt lgkmcnt(8)
	v_mfma_f32_32x32x16_f16 v[16:31], v[140:143], v[96:99], v[16:31]
	v_exp_f32_e32 v80, v80
	v_exp_f32_e32 v81, v81
	v_exp_f32_e32 v82, v82
	v_exp_f32_e32 v83, v83
	v_mfma_f32_32x32x16_f16 v[32:47], v[140:143], v[64:67], v[32:47]
	v_exp_f32_e32 v84, v84
	v_exp_f32_e32 v85, v85
	v_exp_f32_e32 v86, v86
	v_exp_f32_e32 v87, v87
	v_mfma_f32_32x32x16_f16 v[16:31], v[132:135], v[68:71], v[16:31]
	v_exp_f32_e32 v88, v88
	v_exp_f32_e32 v89, v89
	v_exp_f32_e32 v90, v90
	v_exp_f32_e32 v91, v91
	v_mfma_f32_32x32x16_f16 v[32:47], v[132:135], v[72:75], v[32:47]
	v_exp_f32_e32 v92, v92
	v_exp_f32_e32 v93, v93
	v_exp_f32_e32 v94, v94
	v_exp_f32_e32 v95, v95
	s_waitcnt lgkmcnt(0)
	v_mfma_f32_32x32x16_f16 v[16:31], v[124:127], v[76:79], v[16:31]
	v_exp_f32_e32 v0, v0
	v_exp_f32_e32 v1, v1
	v_exp_f32_e32 v2, v2
	v_exp_f32_e32 v3, v3
	v_mfma_f32_32x32x16_f16 v[32:47], v[124:127], v[100:103], v[32:47]
	v_exp_f32_e32 v4, v4
	v_exp_f32_e32 v5, v5
	v_exp_f32_e32 v6, v6
	v_exp_f32_e32 v7, v7
	v_mfma_f32_32x32x16_f16 v[16:31], v[116:119], v[104:107], v[16:31]
	v_exp_f32_e32 v8, v8
	v_exp_f32_e32 v9, v9
	v_exp_f32_e32 v10, v10
	v_exp_f32_e32 v11, v11
	v_mfma_f32_32x32x16_f16 v[32:47], v[116:119], v[108:111], v[32:47]
	v_exp_f32_e32 v12, v12
	v_exp_f32_e32 v13, v13
	v_exp_f32_e32 v14, v14
	v_exp_f32_e32 v15, v15
	v_add_u32_e32 v48, s11, v182
